# router MFMA section of both LN+router phases: expert-weight fragments prefetched one K-step ahead (double-buffered), straight-line
# baseline (speedup 1.0000x reference)
; #define GAS __attribute__((address_space(1)))
; #define LAS __attribute__((address_space(3)))
; __device__ __forceinline__ void phase_ln_router(const Frame& F, const Args& a, int layer) {
;     ...
;         f32x4 acc[3][4];
; #pragma unroll
;         for (int mt = 0; mt < 3; ++mt)
; #pragma unroll
;             for (int nt = 0; nt < 4; ++nt) acc[mt][nt] = (f32x4){0.f, 0.f, 0.f, 0.f};
;         { int arow[3];
; #pragma unroll
;           for (int mt = 0; mt < 3; ++mt) { const int rr = 16 * mt + fr; arow[mt] = (rr < TPB ? rr : TPB - 1) * HB_LD; }
; #pragma unroll 2
;           for (int kk = 0; kk < 8; ++kk) { const int k0 = F.wave * 256 + 32 * kk + 8 * fq;
;               bf16x8 bh[4], af[3];
; #pragma unroll
;               for (int nt = 0; nt < 4; ++nt) bh[nt] = *(const GAS bf16x8*)(rwh + (size_t)(16 * nt + fr) * D + k0);
; #pragma unroll
;               for (int mt = 0; mt < 3; ++mt) af[mt] = *(const LAS bf16x8*)(hb + arow[mt] + k0);
; #pragma unroll
;               for (int mt = 0; mt < 3; ++mt)
; #pragma unroll
;                   for (int nt = 0; nt < 4; ++nt) acc[mt][nt] = __builtin_amdgcn_mfma_f32_16x16x32_bf16(af[mt], bh[nt], acc[mt][nt], 0, 0, 0); } }
.LBB0_1292:
	v_mov_b32_e32 v66, 0
	s_mov_b32 s0, 0
	v_mov_b32_e32 v140, v145
	v_mov_b32_e32 v67, v66
	v_mov_b32_e32 v68, v66
	v_mov_b32_e32 v69, v66
	v_mov_b32_e32 v70, v66
	v_mov_b32_e32 v71, v66
	v_mov_b32_e32 v72, v66
	v_mov_b32_e32 v73, v66
	v_mov_b32_e32 v78, v66
	v_mov_b32_e32 v79, v66
	v_mov_b32_e32 v80, v66
	v_mov_b32_e32 v81, v66
	v_mov_b32_e32 v82, v66
	v_mov_b32_e32 v83, v66
	v_mov_b32_e32 v84, v66
	v_mov_b32_e32 v85, v66
	v_mov_b32_e32 v74, v66
	v_mov_b32_e32 v75, v66
	v_mov_b32_e32 v76, v66
	v_mov_b32_e32 v77, v66
	v_mov_b32_e32 v90, v66
	v_mov_b32_e32 v91, v66
	v_mov_b32_e32 v92, v66
	v_mov_b32_e32 v93, v66
	v_mov_b32_e32 v98, v66
	v_mov_b32_e32 v99, v66
	v_mov_b32_e32 v100, v66
	v_mov_b32_e32 v101, v66
	v_mov_b32_e32 v86, v66
	v_mov_b32_e32 v87, v66
	v_mov_b32_e32 v88, v66
	v_mov_b32_e32 v89, v66
	v_mov_b32_e32 v102, v66
	v_mov_b32_e32 v103, v66
	v_mov_b32_e32 v104, v66
	v_mov_b32_e32 v105, v66
	v_mov_b32_e32 v106, v66
	v_mov_b32_e32 v107, v66
	v_mov_b32_e32 v108, v66
	v_mov_b32_e32 v109, v66
	v_mov_b32_e32 v110, v66
	v_mov_b32_e32 v111, v66
	v_mov_b32_e32 v112, v66
	v_mov_b32_e32 v113, v66
	v_mov_b32_e32 v94, v66
	v_mov_b32_e32 v95, v66
	v_mov_b32_e32 v96, v66
	v_mov_b32_e32 v97, v66
	v_ashrrev_i32_e32 v141, 31, v140
	v_lshl_add_u64 v[130:131], v[140:141], 1, v[116:117]
	v_add_co_u32_e32 v132, vcc, s41, v130
	s_nop 1
	v_addc_co_u32_e32 v133, vcc, 0, v131, vcc
	v_add_co_u32_e32 v134, vcc, s48, v130
	s_nop 1
	v_addc_co_u32_e32 v135, vcc, 0, v131, vcc
	v_add_co_u32_e32 v136, vcc, s49, v130
	s_nop 1
	v_addc_co_u32_e32 v137, vcc, 0, v131, vcc
	v_add_u32_e32 v195, 0x10100, v147
	global_load_dwordx4 v[2:5], v[130:131], off
	global_load_dwordx4 v[6:9], v[130:131], off offset:64
	global_load_dwordx4 v[10:13], v[132:133], off
	global_load_dwordx4 v[14:17], v[132:133], off offset:64
	global_load_dwordx4 v[18:21], v[134:135], off
	global_load_dwordx4 v[22:25], v[134:135], off offset:64
	global_load_dwordx4 v[26:29], v[136:137], off
	global_load_dwordx4 v[30:33], v[136:137], off offset:64
	s_waitcnt lgkmcnt(0)
	s_barrier
	global_load_dwordx4 v[34:37], v[130:131], off offset:128
	global_load_dwordx4 v[38:41], v[130:131], off offset:192
	global_load_dwordx4 v[42:45], v[132:133], off offset:128
	global_load_dwordx4 v[46:49], v[132:133], off offset:192
	global_load_dwordx4 v[50:53], v[134:135], off offset:128
	global_load_dwordx4 v[54:57], v[134:135], off offset:192
	global_load_dwordx4 v[58:61], v[136:137], off offset:128
	global_load_dwordx4 v[62:65], v[136:137], off offset:192
	ds_read_b128 v[164:167], v147
	ds_read_b128 v[176:179], v195
	ds_read_b128 v[180:183], v146
	ds_read_b128 v[168:171], v147 offset:64
	ds_read_b128 v[172:175], v195 offset:64
	ds_read_b128 v[184:187], v146 offset:64
	s_waitcnt vmcnt(8)
	s_waitcnt lgkmcnt(0)
	v_mfma_f32_16x16x32_bf16 v[94:97], v[164:167], v[2:5], v[94:97]
	v_mfma_f32_16x16x32_bf16 v[86:89], v[176:179], v[2:5], v[86:89]
	v_mfma_f32_16x16x32_bf16 v[82:85], v[180:183], v[2:5], v[82:85]
	v_mfma_f32_16x16x32_bf16 v[110:113], v[164:167], v[10:13], v[110:113]
	v_mfma_f32_16x16x32_bf16 v[98:101], v[176:179], v[10:13], v[98:101]
	v_mfma_f32_16x16x32_bf16 v[78:81], v[180:183], v[10:13], v[78:81]
	v_mfma_f32_16x16x32_bf16 v[106:109], v[164:167], v[18:21], v[106:109]
	v_mfma_f32_16x16x32_bf16 v[90:93], v[176:179], v[18:21], v[90:93]
	v_mfma_f32_16x16x32_bf16 v[70:73], v[180:183], v[18:21], v[70:73]
	v_mfma_f32_16x16x32_bf16 v[102:105], v[164:167], v[26:29], v[102:105]
	v_mfma_f32_16x16x32_bf16 v[74:77], v[176:179], v[26:29], v[74:77]
	v_mfma_f32_16x16x32_bf16 v[66:69], v[180:183], v[26:29], v[66:69]
	v_mfma_f32_16x16x32_bf16 v[94:97], v[168:171], v[6:9], v[94:97]
	v_mfma_f32_16x16x32_bf16 v[86:89], v[172:175], v[6:9], v[86:89]
	v_mfma_f32_16x16x32_bf16 v[82:85], v[184:187], v[6:9], v[82:85]
	v_mfma_f32_16x16x32_bf16 v[110:113], v[168:171], v[14:17], v[110:113]
	v_mfma_f32_16x16x32_bf16 v[98:101], v[172:175], v[14:17], v[98:101]
	v_mfma_f32_16x16x32_bf16 v[78:81], v[184:187], v[14:17], v[78:81]
	v_mfma_f32_16x16x32_bf16 v[106:109], v[168:171], v[22:25], v[106:109]
	v_mfma_f32_16x16x32_bf16 v[90:93], v[172:175], v[22:25], v[90:93]
	v_mfma_f32_16x16x32_bf16 v[70:73], v[184:187], v[22:25], v[70:73]
	v_mfma_f32_16x16x32_bf16 v[102:105], v[168:171], v[30:33], v[102:105]
	v_mfma_f32_16x16x32_bf16 v[74:77], v[172:175], v[30:33], v[74:77]
	v_mfma_f32_16x16x32_bf16 v[66:69], v[184:187], v[30:33], v[66:69]
	global_load_dwordx4 v[2:5], v[130:131], off offset:256
	global_load_dwordx4 v[6:9], v[130:131], off offset:320
	global_load_dwordx4 v[10:13], v[132:133], off offset:256
	global_load_dwordx4 v[14:17], v[132:133], off offset:320
	global_load_dwordx4 v[18:21], v[134:135], off offset:256
	global_load_dwordx4 v[22:25], v[134:135], off offset:320
	global_load_dwordx4 v[26:29], v[136:137], off offset:256
	global_load_dwordx4 v[30:33], v[136:137], off offset:320
	ds_read_b128 v[164:167], v147 offset:128
	ds_read_b128 v[176:179], v195 offset:128
	ds_read_b128 v[180:183], v146 offset:128
	ds_read_b128 v[168:171], v147 offset:192
	ds_read_b128 v[172:175], v195 offset:192
	ds_read_b128 v[184:187], v146 offset:192
	s_waitcnt vmcnt(8)
	s_waitcnt lgkmcnt(0)
; #define GAS __attribute__((address_space(1)))
; #define LAS __attribute__((address_space(3)))
; __device__ __forceinline__ void phase_ln_router(const Frame& F, const Args& a, int layer) {
;     ...
;         { int arow[3];
; #pragma unroll
;           for (int mt = 0; mt < 3; ++mt) { const int rr = 16 * mt + fr; arow[mt] = (rr < TPB ? rr : TPB - 1) * HB_LD; }
; #pragma unroll 2
;           for (int kk = 0; kk < 8; ++kk) { const int k0 = F.wave * 256 + 32 * kk + 8 * fq;
;               bf16x8 bh[4], af[3];
; #pragma unroll
;               for (int nt = 0; nt < 4; ++nt) bh[nt] = *(const GAS bf16x8*)(rwh + (size_t)(16 * nt + fr) * D + k0);
; #pragma unroll
;               for (int mt = 0; mt < 3; ++mt) af[mt] = *(const LAS bf16x8*)(hb + arow[mt] + k0);
; #pragma unroll
;               for (int mt = 0; mt < 3; ++mt)
; #pragma unroll
;                   for (int nt = 0; nt < 4; ++nt) acc[mt][nt] = __builtin_amdgcn_mfma_f32_16x16x32_bf16(af[mt], bh[nt], acc[mt][nt], 0, 0, 0); } }
;         __syncthreads();
	v_mfma_f32_16x16x32_bf16 v[94:97], v[164:167], v[34:37], v[94:97]
	v_mfma_f32_16x16x32_bf16 v[86:89], v[176:179], v[34:37], v[86:89]
	v_mfma_f32_16x16x32_bf16 v[82:85], v[180:183], v[34:37], v[82:85]
	v_mfma_f32_16x16x32_bf16 v[110:113], v[164:167], v[42:45], v[110:113]
	v_mfma_f32_16x16x32_bf16 v[98:101], v[176:179], v[42:45], v[98:101]
	v_mfma_f32_16x16x32_bf16 v[78:81], v[180:183], v[42:45], v[78:81]
	v_mfma_f32_16x16x32_bf16 v[106:109], v[164:167], v[50:53], v[106:109]
	v_mfma_f32_16x16x32_bf16 v[90:93], v[176:179], v[50:53], v[90:93]
	v_mfma_f32_16x16x32_bf16 v[70:73], v[180:183], v[50:53], v[70:73]
	v_mfma_f32_16x16x32_bf16 v[102:105], v[164:167], v[58:61], v[102:105]
	v_mfma_f32_16x16x32_bf16 v[74:77], v[176:179], v[58:61], v[74:77]
	v_mfma_f32_16x16x32_bf16 v[66:69], v[180:183], v[58:61], v[66:69]
	v_mfma_f32_16x16x32_bf16 v[94:97], v[168:171], v[38:41], v[94:97]
	v_mfma_f32_16x16x32_bf16 v[86:89], v[172:175], v[38:41], v[86:89]
	v_mfma_f32_16x16x32_bf16 v[82:85], v[184:187], v[38:41], v[82:85]
	v_mfma_f32_16x16x32_bf16 v[110:113], v[168:171], v[46:49], v[110:113]
	v_mfma_f32_16x16x32_bf16 v[98:101], v[172:175], v[46:49], v[98:101]
	v_mfma_f32_16x16x32_bf16 v[78:81], v[184:187], v[46:49], v[78:81]
	v_mfma_f32_16x16x32_bf16 v[106:109], v[168:171], v[54:57], v[106:109]
	v_mfma_f32_16x16x32_bf16 v[90:93], v[172:175], v[54:57], v[90:93]
	v_mfma_f32_16x16x32_bf16 v[70:73], v[184:187], v[54:57], v[70:73]
	v_mfma_f32_16x16x32_bf16 v[102:105], v[168:171], v[62:65], v[102:105]
	v_mfma_f32_16x16x32_bf16 v[74:77], v[172:175], v[62:65], v[74:77]
	v_mfma_f32_16x16x32_bf16 v[66:69], v[184:187], v[62:65], v[66:69]
	global_load_dwordx4 v[34:37], v[130:131], off offset:384
	global_load_dwordx4 v[38:41], v[130:131], off offset:448
	global_load_dwordx4 v[42:45], v[132:133], off offset:384
	global_load_dwordx4 v[46:49], v[132:133], off offset:448
	global_load_dwordx4 v[50:53], v[134:135], off offset:384
	global_load_dwordx4 v[54:57], v[134:135], off offset:448
	global_load_dwordx4 v[58:61], v[136:137], off offset:384
	global_load_dwordx4 v[62:65], v[136:137], off offset:448
	ds_read_b128 v[164:167], v147 offset:256
	ds_read_b128 v[176:179], v195 offset:256
	ds_read_b128 v[180:183], v146 offset:256
	ds_read_b128 v[168:171], v147 offset:320
	ds_read_b128 v[172:175], v195 offset:320
	ds_read_b128 v[184:187], v146 offset:320
	s_waitcnt vmcnt(8)
	s_waitcnt lgkmcnt(0)
	v_mfma_f32_16x16x32_bf16 v[94:97], v[164:167], v[2:5], v[94:97]
	v_mfma_f32_16x16x32_bf16 v[86:89], v[176:179], v[2:5], v[86:89]
	v_mfma_f32_16x16x32_bf16 v[82:85], v[180:183], v[2:5], v[82:85]
	v_mfma_f32_16x16x32_bf16 v[110:113], v[164:167], v[10:13], v[110:113]
	v_mfma_f32_16x16x32_bf16 v[98:101], v[176:179], v[10:13], v[98:101]
	v_mfma_f32_16x16x32_bf16 v[78:81], v[180:183], v[10:13], v[78:81]
	v_mfma_f32_16x16x32_bf16 v[106:109], v[164:167], v[18:21], v[106:109]
	v_mfma_f32_16x16x32_bf16 v[90:93], v[176:179], v[18:21], v[90:93]
	v_mfma_f32_16x16x32_bf16 v[70:73], v[180:183], v[18:21], v[70:73]
	v_mfma_f32_16x16x32_bf16 v[102:105], v[164:167], v[26:29], v[102:105]
	v_mfma_f32_16x16x32_bf16 v[74:77], v[176:179], v[26:29], v[74:77]
	v_mfma_f32_16x16x32_bf16 v[66:69], v[180:183], v[26:29], v[66:69]
	v_mfma_f32_16x16x32_bf16 v[94:97], v[168:171], v[6:9], v[94:97]
	v_mfma_f32_16x16x32_bf16 v[86:89], v[172:175], v[6:9], v[86:89]
	v_mfma_f32_16x16x32_bf16 v[82:85], v[184:187], v[6:9], v[82:85]
	v_mfma_f32_16x16x32_bf16 v[110:113], v[168:171], v[14:17], v[110:113]
	v_mfma_f32_16x16x32_bf16 v[98:101], v[172:175], v[14:17], v[98:101]
	v_mfma_f32_16x16x32_bf16 v[78:81], v[184:187], v[14:17], v[78:81]
	v_mfma_f32_16x16x32_bf16 v[106:109], v[168:171], v[22:25], v[106:109]
	v_mfma_f32_16x16x32_bf16 v[90:93], v[172:175], v[22:25], v[90:93]
	v_mfma_f32_16x16x32_bf16 v[70:73], v[184:187], v[22:25], v[70:73]
	v_mfma_f32_16x16x32_bf16 v[102:105], v[168:171], v[30:33], v[102:105]
	v_mfma_f32_16x16x32_bf16 v[74:77], v[172:175], v[30:33], v[74:77]
	v_mfma_f32_16x16x32_bf16 v[66:69], v[184:187], v[30:33], v[66:69]
	ds_read_b128 v[164:167], v147 offset:384
	ds_read_b128 v[176:179], v195 offset:384
	ds_read_b128 v[180:183], v146 offset:384
	ds_read_b128 v[168:171], v147 offset:448
	ds_read_b128 v[172:175], v195 offset:448
	ds_read_b128 v[184:187], v146 offset:448
	s_waitcnt vmcnt(0)
	s_waitcnt lgkmcnt(0)
	v_mfma_f32_16x16x32_bf16 v[94:97], v[164:167], v[34:37], v[94:97]
	v_mfma_f32_16x16x32_bf16 v[86:89], v[176:179], v[34:37], v[86:89]
	v_mfma_f32_16x16x32_bf16 v[82:85], v[180:183], v[34:37], v[82:85]
	v_mfma_f32_16x16x32_bf16 v[110:113], v[164:167], v[42:45], v[110:113]
	v_mfma_f32_16x16x32_bf16 v[98:101], v[176:179], v[42:45], v[98:101]
	v_mfma_f32_16x16x32_bf16 v[78:81], v[180:183], v[42:45], v[78:81]
	v_mfma_f32_16x16x32_bf16 v[106:109], v[164:167], v[50:53], v[106:109]
	v_mfma_f32_16x16x32_bf16 v[90:93], v[176:179], v[50:53], v[90:93]
	v_mfma_f32_16x16x32_bf16 v[70:73], v[180:183], v[50:53], v[70:73]
	v_mfma_f32_16x16x32_bf16 v[102:105], v[164:167], v[58:61], v[102:105]
	v_mfma_f32_16x16x32_bf16 v[74:77], v[176:179], v[58:61], v[74:77]
	v_mfma_f32_16x16x32_bf16 v[66:69], v[180:183], v[58:61], v[66:69]
	v_mfma_f32_16x16x32_bf16 v[94:97], v[168:171], v[38:41], v[94:97]
	v_mfma_f32_16x16x32_bf16 v[86:89], v[172:175], v[38:41], v[86:89]
	v_mfma_f32_16x16x32_bf16 v[82:85], v[184:187], v[38:41], v[82:85]
	v_mfma_f32_16x16x32_bf16 v[110:113], v[168:171], v[46:49], v[110:113]
	v_mfma_f32_16x16x32_bf16 v[98:101], v[172:175], v[46:49], v[98:101]
	v_mfma_f32_16x16x32_bf16 v[78:81], v[184:187], v[46:49], v[78:81]
	v_mfma_f32_16x16x32_bf16 v[106:109], v[168:171], v[54:57], v[106:109]
	v_mfma_f32_16x16x32_bf16 v[90:93], v[172:175], v[54:57], v[90:93]
	v_mfma_f32_16x16x32_bf16 v[70:73], v[184:187], v[54:57], v[70:73]
	v_mfma_f32_16x16x32_bf16 v[102:105], v[168:171], v[62:65], v[102:105]
	v_mfma_f32_16x16x32_bf16 v[74:77], v[172:175], v[62:65], v[74:77]
	v_mfma_f32_16x16x32_bf16 v[66:69], v[184:187], v[62:65], v[66:69]
	s_movk_i32 s0, 0x200
	s_barrier
; __device__ __forceinline__ void phase_ln_router(const Frame& F, const Args& a, int layer) {
;     ...
;         __syncthreads();
; #pragma unroll
;         for (int mt = 0; mt < 3; ++mt)
; #pragma unroll
;             for (int nt = 0; nt < 4; ++nt)
; #pragma unroll
;                 for (int j = 0; j < 4; ++j) part[(F.wave * 48 + 16 * mt + 4 * fq + j) * 64 + 16 * nt + fr] = acc[mt][nt][j];
;         __syncthreads();
	ds_write2_b32 v156, v94, v110 offset1:16
	ds_write2_b32 v156, v95, v111 offset0:64 offset1:80
	ds_write2_b32 v156, v96, v112 offset0:128 offset1:144
	ds_write2_b32 v156, v97, v113 offset0:192 offset1:208
	ds_write2_b32 v156, v106, v102 offset0:32 offset1:48
	ds_write2_b32 v156, v107, v103 offset0:96 offset1:112
	ds_write2_b32 v156, v108, v104 offset0:160 offset1:176
	ds_write2_b32 v156, v109, v105 offset0:224 offset1:240
	v_add_u32_e32 v94, 0x1000, v156
	ds_write2_b32 v94, v86, v98 offset1:16
	ds_write2_b32 v94, v87, v99 offset0:64 offset1:80
	ds_write2_b32 v94, v88, v100 offset0:128 offset1:144
	ds_write2_b32 v94, v89, v101 offset0:192 offset1:208
	ds_write2_b32 v94, v90, v74 offset0:32 offset1:48
	ds_write2_b32 v94, v91, v75 offset0:96 offset1:112
	ds_write2_b32 v94, v92, v76 offset0:160 offset1:176
	ds_write2_b32 v94, v93, v77 offset0:224 offset1:240
	v_add_u32_e32 v74, 0x2000, v156
	ds_write2_b32 v74, v82, v78 offset1:16
	ds_write2_b32 v74, v83, v79 offset0:64 offset1:80
	ds_write2_b32 v74, v84, v80 offset0:128 offset1:144
	ds_write2_b32 v74, v85, v81 offset0:192 offset1:208
	ds_write2_b32 v74, v70, v66 offset0:32 offset1:48
	ds_write2_b32 v74, v71, v67 offset0:96 offset1:112
	ds_write2_b32 v74, v72, v68 offset0:160 offset1:176
	ds_write2_b32 v74, v73, v69 offset0:224 offset1:240
	v_mov_b32_e32 v66, 0
	s_and_b64 vcc, exec, s[44:45]
	s_waitcnt lgkmcnt(0)
	s_barrier
	s_cbranch_vccz .LBB0_1334
	v_and_b32_e32 v67, 64, v158
	v_add_u32_e32 v72, 64, v67
	v_xor_b32_e32 v67, 1, v158
	v_cmp_lt_i32_e32 vcc, v67, v72
	v_xor_b32_e32 v68, 2, v158
	v_xor_b32_e32 v69, 4, v158
	v_cndmask_b32_e32 v67, v158, v67, vcc
	v_cmp_lt_i32_e32 vcc, v68, v72
	v_xor_b32_e32 v70, 8, v158
	v_xor_b32_e32 v71, 16, v158
	v_cndmask_b32_e32 v68, v158, v68, vcc
	v_cmp_lt_i32_e32 vcc, v69, v72
	v_xor_b32_e32 v73, 32, v158
	v_mov_b32_e32 v66, 0
	v_cndmask_b32_e32 v69, v158, v69, vcc
	v_cmp_lt_i32_e32 vcc, v70, v72
	v_lshlrev_b32_e32 v67, 2, v67
	v_lshlrev_b32_e32 v68, 2, v68
	v_cndmask_b32_e32 v70, v158, v70, vcc
	v_cmp_lt_i32_e32 vcc, v71, v72
	v_lshlrev_b32_e32 v69, 2, v69
	v_lshlrev_b32_e32 v70, 2, v70
	v_cndmask_b32_e32 v71, v158, v71, vcc
	v_cmp_lt_i32_e32 vcc, v73, v72
	v_lshlrev_b32_e32 v71, 2, v71
	s_mov_b32 s2, s74
	v_cndmask_b32_e32 v72, v158, v73, vcc
	v_lshlrev_b32_e32 v72, 2, v72

; #define GAS __attribute__((address_space(1)))
; #define LAS __attribute__((address_space(3)))
; __device__ __forceinline__ void phase_ln_router(const Frame& F, const Args& a, int layer) {
;     ...
;         f32x4 acc[3][4];
; #pragma unroll
;         for (int mt = 0; mt < 3; ++mt)
; #pragma unroll
;             for (int nt = 0; nt < 4; ++nt) acc[mt][nt] = (f32x4){0.f, 0.f, 0.f, 0.f};
;         { int arow[3];
; #pragma unroll
;           for (int mt = 0; mt < 3; ++mt) { const int rr = 16 * mt + fr; arow[mt] = (rr < TPB ? rr : TPB - 1) * HB_LD; }
; #pragma unroll 2
;           for (int kk = 0; kk < 8; ++kk) { const int k0 = F.wave * 256 + 32 * kk + 8 * fq;
;               bf16x8 bh[4], af[3];
; #pragma unroll
;               for (int nt = 0; nt < 4; ++nt) bh[nt] = *(const GAS bf16x8*)(rwh + (size_t)(16 * nt + fr) * D + k0);
; #pragma unroll
;               for (int mt = 0; mt < 3; ++mt) af[mt] = *(const LAS bf16x8*)(hb + arow[mt] + k0);
; #pragma unroll
;               for (int mt = 0; mt < 3; ++mt)
; #pragma unroll
;                   for (int nt = 0; nt < 4; ++nt) acc[mt][nt] = __builtin_amdgcn_mfma_f32_16x16x32_bf16(af[mt], bh[nt], acc[mt][nt], 0, 0, 0); } }
.LBB0_3038:
	v_mov_b32_e32 v66, 0
	s_mov_b32 s0, 0
	v_mov_b32_e32 v152, v157
	v_mov_b32_e32 v67, v66
	v_mov_b32_e32 v68, v66
	v_mov_b32_e32 v69, v66
	v_mov_b32_e32 v70, v66
	v_mov_b32_e32 v71, v66
	v_mov_b32_e32 v72, v66
	v_mov_b32_e32 v73, v66
	v_mov_b32_e32 v74, v66
	v_mov_b32_e32 v75, v66
	v_mov_b32_e32 v76, v66
	v_mov_b32_e32 v77, v66
	v_mov_b32_e32 v82, v66
	v_mov_b32_e32 v83, v66
	v_mov_b32_e32 v84, v66
	v_mov_b32_e32 v85, v66
	v_mov_b32_e32 v78, v66
	v_mov_b32_e32 v79, v66
	v_mov_b32_e32 v80, v66
	v_mov_b32_e32 v81, v66
	v_mov_b32_e32 v90, v66
	v_mov_b32_e32 v91, v66
	v_mov_b32_e32 v92, v66
	v_mov_b32_e32 v93, v66
	v_mov_b32_e32 v98, v66
	v_mov_b32_e32 v99, v66
	v_mov_b32_e32 v100, v66
	v_mov_b32_e32 v101, v66
	v_mov_b32_e32 v86, v66
	v_mov_b32_e32 v87, v66
	v_mov_b32_e32 v88, v66
	v_mov_b32_e32 v89, v66
	v_mov_b32_e32 v102, v66
	v_mov_b32_e32 v103, v66
	v_mov_b32_e32 v104, v66
	v_mov_b32_e32 v105, v66
	v_mov_b32_e32 v106, v66
	v_mov_b32_e32 v107, v66
	v_mov_b32_e32 v108, v66
	v_mov_b32_e32 v109, v66
	v_mov_b32_e32 v110, v66
	v_mov_b32_e32 v111, v66
	v_mov_b32_e32 v112, v66
	v_mov_b32_e32 v113, v66
	v_mov_b32_e32 v94, v66
	v_mov_b32_e32 v95, v66
	v_mov_b32_e32 v96, v66
	v_mov_b32_e32 v97, v66
	v_ashrrev_i32_e32 v153, 31, v152
	v_lshl_add_u64 v[142:143], v[152:153], 1, v[116:117]
	v_add_co_u32_e32 v144, vcc, s51, v142
	s_nop 1
	v_addc_co_u32_e32 v145, vcc, 0, v143, vcc
	v_add_co_u32_e32 v146, vcc, s52, v142
	s_nop 1
	v_addc_co_u32_e32 v147, vcc, 0, v143, vcc
	v_add_co_u32_e32 v148, vcc, s53, v142
	s_nop 1
	v_addc_co_u32_e32 v149, vcc, 0, v143, vcc
	v_add_u32_e32 v246, 0x10100, v159
	v_add_u32_e32 v247, 0x1f1f0, v158
	global_load_dwordx4 v[2:5], v[142:143], off
	global_load_dwordx4 v[6:9], v[142:143], off offset:64
	global_load_dwordx4 v[10:13], v[144:145], off
	global_load_dwordx4 v[14:17], v[144:145], off offset:64
	global_load_dwordx4 v[18:21], v[146:147], off
	global_load_dwordx4 v[22:25], v[146:147], off offset:64
	global_load_dwordx4 v[26:29], v[148:149], off
	global_load_dwordx4 v[30:33], v[148:149], off offset:64
	s_waitcnt lgkmcnt(0)
	s_barrier
	global_load_dwordx4 v[34:37], v[142:143], off offset:128
	global_load_dwordx4 v[38:41], v[142:143], off offset:192
	global_load_dwordx4 v[42:45], v[144:145], off offset:128
	global_load_dwordx4 v[46:49], v[144:145], off offset:192
	global_load_dwordx4 v[50:53], v[146:147], off offset:128
	global_load_dwordx4 v[54:57], v[146:147], off offset:192
	global_load_dwordx4 v[58:61], v[148:149], off offset:128
	global_load_dwordx4 v[62:65], v[148:149], off offset:192
	ds_read_b128 v[176:179], v159
	ds_read_b128 v[188:191], v246
	ds_read_b128 v[192:195], v247
	ds_read_b128 v[180:183], v159 offset:64
	ds_read_b128 v[184:187], v246 offset:64
	ds_read_b128 v[196:199], v247 offset:64
	s_waitcnt vmcnt(8)
	s_waitcnt lgkmcnt(0)
	v_mfma_f32_16x16x32_bf16 v[94:97], v[176:179], v[2:5], v[94:97]
	v_mfma_f32_16x16x32_bf16 v[86:89], v[188:191], v[2:5], v[86:89]
	v_mfma_f32_16x16x32_bf16 v[82:85], v[192:195], v[2:5], v[82:85]
	v_mfma_f32_16x16x32_bf16 v[110:113], v[176:179], v[10:13], v[110:113]
	v_mfma_f32_16x16x32_bf16 v[98:101], v[188:191], v[10:13], v[98:101]
	v_mfma_f32_16x16x32_bf16 v[74:77], v[192:195], v[10:13], v[74:77]
	v_mfma_f32_16x16x32_bf16 v[106:109], v[176:179], v[18:21], v[106:109]
	v_mfma_f32_16x16x32_bf16 v[90:93], v[188:191], v[18:21], v[90:93]
	v_mfma_f32_16x16x32_bf16 v[70:73], v[192:195], v[18:21], v[70:73]
	v_mfma_f32_16x16x32_bf16 v[102:105], v[176:179], v[26:29], v[102:105]
	v_mfma_f32_16x16x32_bf16 v[78:81], v[188:191], v[26:29], v[78:81]
	v_mfma_f32_16x16x32_bf16 v[66:69], v[192:195], v[26:29], v[66:69]
	v_mfma_f32_16x16x32_bf16 v[94:97], v[180:183], v[6:9], v[94:97]
	v_mfma_f32_16x16x32_bf16 v[86:89], v[184:187], v[6:9], v[86:89]
	v_mfma_f32_16x16x32_bf16 v[82:85], v[196:199], v[6:9], v[82:85]
	v_mfma_f32_16x16x32_bf16 v[110:113], v[180:183], v[14:17], v[110:113]
	v_mfma_f32_16x16x32_bf16 v[98:101], v[184:187], v[14:17], v[98:101]
	v_mfma_f32_16x16x32_bf16 v[74:77], v[196:199], v[14:17], v[74:77]
	v_mfma_f32_16x16x32_bf16 v[106:109], v[180:183], v[22:25], v[106:109]
	v_mfma_f32_16x16x32_bf16 v[90:93], v[184:187], v[22:25], v[90:93]
	v_mfma_f32_16x16x32_bf16 v[70:73], v[196:199], v[22:25], v[70:73]
	v_mfma_f32_16x16x32_bf16 v[102:105], v[180:183], v[30:33], v[102:105]
	v_mfma_f32_16x16x32_bf16 v[78:81], v[184:187], v[30:33], v[78:81]
	v_mfma_f32_16x16x32_bf16 v[66:69], v[196:199], v[30:33], v[66:69]
	global_load_dwordx4 v[2:5], v[142:143], off offset:256
	global_load_dwordx4 v[6:9], v[142:143], off offset:320
	global_load_dwordx4 v[10:13], v[144:145], off offset:256
	global_load_dwordx4 v[14:17], v[144:145], off offset:320
	global_load_dwordx4 v[18:21], v[146:147], off offset:256
	global_load_dwordx4 v[22:25], v[146:147], off offset:320
	global_load_dwordx4 v[26:29], v[148:149], off offset:256
	global_load_dwordx4 v[30:33], v[148:149], off offset:320
	ds_read_b128 v[176:179], v159 offset:128
	ds_read_b128 v[188:191], v246 offset:128
	ds_read_b128 v[192:195], v247 offset:128
	ds_read_b128 v[180:183], v159 offset:192
	ds_read_b128 v[184:187], v246 offset:192
	ds_read_b128 v[196:199], v247 offset:192
	s_waitcnt vmcnt(8)
	s_waitcnt lgkmcnt(0)
; #define GAS __attribute__((address_space(1)))
; #define LAS __attribute__((address_space(3)))
; __device__ __forceinline__ void phase_ln_router(const Frame& F, const Args& a, int layer) {
;     ...
;         { int arow[3];
; #pragma unroll
;           for (int mt = 0; mt < 3; ++mt) { const int rr = 16 * mt + fr; arow[mt] = (rr < TPB ? rr : TPB - 1) * HB_LD; }
; #pragma unroll 2
;           for (int kk = 0; kk < 8; ++kk) { const int k0 = F.wave * 256 + 32 * kk + 8 * fq;
;               bf16x8 bh[4], af[3];
; #pragma unroll
;               for (int nt = 0; nt < 4; ++nt) bh[nt] = *(const GAS bf16x8*)(rwh + (size_t)(16 * nt + fr) * D + k0);
; #pragma unroll
;               for (int mt = 0; mt < 3; ++mt) af[mt] = *(const LAS bf16x8*)(hb + arow[mt] + k0);
; #pragma unroll
;               for (int mt = 0; mt < 3; ++mt)
; #pragma unroll
;                   for (int nt = 0; nt < 4; ++nt) acc[mt][nt] = __builtin_amdgcn_mfma_f32_16x16x32_bf16(af[mt], bh[nt], acc[mt][nt], 0, 0, 0); } }
;         __syncthreads();
	v_mfma_f32_16x16x32_bf16 v[94:97], v[176:179], v[34:37], v[94:97]
	v_mfma_f32_16x16x32_bf16 v[86:89], v[188:191], v[34:37], v[86:89]
	v_mfma_f32_16x16x32_bf16 v[82:85], v[192:195], v[34:37], v[82:85]
	v_mfma_f32_16x16x32_bf16 v[110:113], v[176:179], v[42:45], v[110:113]
	v_mfma_f32_16x16x32_bf16 v[98:101], v[188:191], v[42:45], v[98:101]
	v_mfma_f32_16x16x32_bf16 v[74:77], v[192:195], v[42:45], v[74:77]
	v_mfma_f32_16x16x32_bf16 v[106:109], v[176:179], v[50:53], v[106:109]
	v_mfma_f32_16x16x32_bf16 v[90:93], v[188:191], v[50:53], v[90:93]
	v_mfma_f32_16x16x32_bf16 v[70:73], v[192:195], v[50:53], v[70:73]
	v_mfma_f32_16x16x32_bf16 v[102:105], v[176:179], v[58:61], v[102:105]
	v_mfma_f32_16x16x32_bf16 v[78:81], v[188:191], v[58:61], v[78:81]
	v_mfma_f32_16x16x32_bf16 v[66:69], v[192:195], v[58:61], v[66:69]
	v_mfma_f32_16x16x32_bf16 v[94:97], v[180:183], v[38:41], v[94:97]
	v_mfma_f32_16x16x32_bf16 v[86:89], v[184:187], v[38:41], v[86:89]
	v_mfma_f32_16x16x32_bf16 v[82:85], v[196:199], v[38:41], v[82:85]
	v_mfma_f32_16x16x32_bf16 v[110:113], v[180:183], v[46:49], v[110:113]
	v_mfma_f32_16x16x32_bf16 v[98:101], v[184:187], v[46:49], v[98:101]
	v_mfma_f32_16x16x32_bf16 v[74:77], v[196:199], v[46:49], v[74:77]
	v_mfma_f32_16x16x32_bf16 v[106:109], v[180:183], v[54:57], v[106:109]
	v_mfma_f32_16x16x32_bf16 v[90:93], v[184:187], v[54:57], v[90:93]
	v_mfma_f32_16x16x32_bf16 v[70:73], v[196:199], v[54:57], v[70:73]
	v_mfma_f32_16x16x32_bf16 v[102:105], v[180:183], v[62:65], v[102:105]
	v_mfma_f32_16x16x32_bf16 v[78:81], v[184:187], v[62:65], v[78:81]
	v_mfma_f32_16x16x32_bf16 v[66:69], v[196:199], v[62:65], v[66:69]
	global_load_dwordx4 v[34:37], v[142:143], off offset:384
	global_load_dwordx4 v[38:41], v[142:143], off offset:448
	global_load_dwordx4 v[42:45], v[144:145], off offset:384
	global_load_dwordx4 v[46:49], v[144:145], off offset:448
	global_load_dwordx4 v[50:53], v[146:147], off offset:384
	global_load_dwordx4 v[54:57], v[146:147], off offset:448
	global_load_dwordx4 v[58:61], v[148:149], off offset:384
	global_load_dwordx4 v[62:65], v[148:149], off offset:448
	ds_read_b128 v[176:179], v159 offset:256
	ds_read_b128 v[188:191], v246 offset:256
	ds_read_b128 v[192:195], v247 offset:256
	ds_read_b128 v[180:183], v159 offset:320
	ds_read_b128 v[184:187], v246 offset:320
	ds_read_b128 v[196:199], v247 offset:320
	s_waitcnt vmcnt(8)
	s_waitcnt lgkmcnt(0)
	v_mfma_f32_16x16x32_bf16 v[94:97], v[176:179], v[2:5], v[94:97]
	v_mfma_f32_16x16x32_bf16 v[86:89], v[188:191], v[2:5], v[86:89]
	v_mfma_f32_16x16x32_bf16 v[82:85], v[192:195], v[2:5], v[82:85]
	v_mfma_f32_16x16x32_bf16 v[110:113], v[176:179], v[10:13], v[110:113]
	v_mfma_f32_16x16x32_bf16 v[98:101], v[188:191], v[10:13], v[98:101]
	v_mfma_f32_16x16x32_bf16 v[74:77], v[192:195], v[10:13], v[74:77]
	v_mfma_f32_16x16x32_bf16 v[106:109], v[176:179], v[18:21], v[106:109]
	v_mfma_f32_16x16x32_bf16 v[90:93], v[188:191], v[18:21], v[90:93]
	v_mfma_f32_16x16x32_bf16 v[70:73], v[192:195], v[18:21], v[70:73]
	v_mfma_f32_16x16x32_bf16 v[102:105], v[176:179], v[26:29], v[102:105]
	v_mfma_f32_16x16x32_bf16 v[78:81], v[188:191], v[26:29], v[78:81]
	v_mfma_f32_16x16x32_bf16 v[66:69], v[192:195], v[26:29], v[66:69]
	v_mfma_f32_16x16x32_bf16 v[94:97], v[180:183], v[6:9], v[94:97]
	v_mfma_f32_16x16x32_bf16 v[86:89], v[184:187], v[6:9], v[86:89]
	v_mfma_f32_16x16x32_bf16 v[82:85], v[196:199], v[6:9], v[82:85]
	v_mfma_f32_16x16x32_bf16 v[110:113], v[180:183], v[14:17], v[110:113]
	v_mfma_f32_16x16x32_bf16 v[98:101], v[184:187], v[14:17], v[98:101]
	v_mfma_f32_16x16x32_bf16 v[74:77], v[196:199], v[14:17], v[74:77]
	v_mfma_f32_16x16x32_bf16 v[106:109], v[180:183], v[22:25], v[106:109]
	v_mfma_f32_16x16x32_bf16 v[90:93], v[184:187], v[22:25], v[90:93]
	v_mfma_f32_16x16x32_bf16 v[70:73], v[196:199], v[22:25], v[70:73]
	v_mfma_f32_16x16x32_bf16 v[102:105], v[180:183], v[30:33], v[102:105]
	v_mfma_f32_16x16x32_bf16 v[78:81], v[184:187], v[30:33], v[78:81]
	v_mfma_f32_16x16x32_bf16 v[66:69], v[196:199], v[30:33], v[66:69]
	ds_read_b128 v[176:179], v159 offset:384
	ds_read_b128 v[188:191], v246 offset:384
	ds_read_b128 v[192:195], v247 offset:384
	ds_read_b128 v[180:183], v159 offset:448
	ds_read_b128 v[184:187], v246 offset:448
	ds_read_b128 v[196:199], v247 offset:448
	s_waitcnt vmcnt(0)
	s_waitcnt lgkmcnt(0)
	v_mfma_f32_16x16x32_bf16 v[94:97], v[176:179], v[34:37], v[94:97]
	v_mfma_f32_16x16x32_bf16 v[86:89], v[188:191], v[34:37], v[86:89]
	v_mfma_f32_16x16x32_bf16 v[82:85], v[192:195], v[34:37], v[82:85]
	v_mfma_f32_16x16x32_bf16 v[110:113], v[176:179], v[42:45], v[110:113]
	v_mfma_f32_16x16x32_bf16 v[98:101], v[188:191], v[42:45], v[98:101]
	v_mfma_f32_16x16x32_bf16 v[74:77], v[192:195], v[42:45], v[74:77]
	v_mfma_f32_16x16x32_bf16 v[106:109], v[176:179], v[50:53], v[106:109]
	v_mfma_f32_16x16x32_bf16 v[90:93], v[188:191], v[50:53], v[90:93]
	v_mfma_f32_16x16x32_bf16 v[70:73], v[192:195], v[50:53], v[70:73]
	v_mfma_f32_16x16x32_bf16 v[102:105], v[176:179], v[58:61], v[102:105]
	v_mfma_f32_16x16x32_bf16 v[78:81], v[188:191], v[58:61], v[78:81]
	v_mfma_f32_16x16x32_bf16 v[66:69], v[192:195], v[58:61], v[66:69]
	v_mfma_f32_16x16x32_bf16 v[94:97], v[180:183], v[38:41], v[94:97]
	v_mfma_f32_16x16x32_bf16 v[86:89], v[184:187], v[38:41], v[86:89]
	v_mfma_f32_16x16x32_bf16 v[82:85], v[196:199], v[38:41], v[82:85]
	v_mfma_f32_16x16x32_bf16 v[110:113], v[180:183], v[46:49], v[110:113]
	v_mfma_f32_16x16x32_bf16 v[98:101], v[184:187], v[46:49], v[98:101]
	v_mfma_f32_16x16x32_bf16 v[74:77], v[196:199], v[46:49], v[74:77]
	v_mfma_f32_16x16x32_bf16 v[106:109], v[180:183], v[54:57], v[106:109]
	v_mfma_f32_16x16x32_bf16 v[90:93], v[184:187], v[54:57], v[90:93]
	v_mfma_f32_16x16x32_bf16 v[70:73], v[196:199], v[54:57], v[70:73]
	v_mfma_f32_16x16x32_bf16 v[102:105], v[180:183], v[62:65], v[102:105]
	v_mfma_f32_16x16x32_bf16 v[78:81], v[184:187], v[62:65], v[78:81]
	v_mfma_f32_16x16x32_bf16 v[66:69], v[196:199], v[62:65], v[66:69]
	s_movk_i32 s0, 0x200
	s_barrier
; __device__ __forceinline__ void phase_ln_router(const Frame& F, const Args& a, int layer) {
;     ...
;         __syncthreads();
; #pragma unroll
;         for (int mt = 0; mt < 3; ++mt)
; #pragma unroll
;             for (int nt = 0; nt < 4; ++nt)
; #pragma unroll
;                 for (int j = 0; j < 4; ++j) part[(F.wave * 48 + 16 * mt + 4 * fq + j) * 64 + 16 * nt + fr] = acc[mt][nt][j];
;         __syncthreads();
	ds_write2_b32 v168, v94, v110 offset1:16
	ds_write2_b32 v168, v95, v111 offset0:64 offset1:80
	ds_write2_b32 v168, v96, v112 offset0:128 offset1:144
	ds_write2_b32 v168, v97, v113 offset0:192 offset1:208
	ds_write2_b32 v168, v106, v102 offset0:32 offset1:48
	ds_write2_b32 v168, v107, v103 offset0:96 offset1:112
	ds_write2_b32 v168, v108, v104 offset0:160 offset1:176
	ds_write2_b32 v168, v109, v105 offset0:224 offset1:240
	v_add_u32_e32 v94, 0x1000, v168
	ds_write2_b32 v94, v86, v98 offset1:16
	ds_write2_b32 v94, v87, v99 offset0:64 offset1:80
	ds_write2_b32 v94, v88, v100 offset0:128 offset1:144
	ds_write2_b32 v94, v89, v101 offset0:192 offset1:208
	ds_write2_b32 v94, v90, v78 offset0:32 offset1:48
	ds_write2_b32 v94, v91, v79 offset0:96 offset1:112
	ds_write2_b32 v94, v92, v80 offset0:160 offset1:176
	ds_write2_b32 v94, v93, v81 offset0:224 offset1:240
	v_add_u32_e32 v78, 0x2000, v168
	ds_write2_b32 v78, v82, v74 offset1:16
	ds_write2_b32 v78, v83, v75 offset0:64 offset1:80
	ds_write2_b32 v78, v84, v76 offset0:128 offset1:144
	ds_write2_b32 v78, v85, v77 offset0:192 offset1:208
	ds_write2_b32 v78, v70, v66 offset0:32 offset1:48
	ds_write2_b32 v78, v71, v67 offset0:96 offset1:112
	ds_write2_b32 v78, v72, v68 offset0:160 offset1:176
	ds_write2_b32 v78, v73, v69 offset0:224 offset1:240
	v_mov_b32_e32 v66, 0
	s_and_b64 vcc, exec, s[44:45]
	s_waitcnt lgkmcnt(0)
	s_barrier
	s_cbranch_vccz .LBB0_3080
	v_and_b32_e32 v67, 64, v170
	v_add_u32_e32 v72, 64, v67
	v_xor_b32_e32 v67, 1, v170
	v_cmp_lt_i32_e32 vcc, v67, v72
	v_xor_b32_e32 v68, 2, v170
	v_xor_b32_e32 v69, 4, v170
	v_cndmask_b32_e32 v67, v170, v67, vcc
	v_cmp_lt_i32_e32 vcc, v68, v72
	v_xor_b32_e32 v70, 8, v170
	v_xor_b32_e32 v71, 16, v170
	v_cndmask_b32_e32 v68, v170, v68, vcc
	v_cmp_lt_i32_e32 vcc, v69, v72
	v_xor_b32_e32 v73, 32, v170
	s_lshl_b32 s2, s57, 5
	v_cndmask_b32_e32 v69, v170, v69, vcc
	v_cmp_lt_i32_e32 vcc, v70, v72
	s_addk_i32 s2, 0x200
	v_mov_b32_e32 v66, 0
	v_cndmask_b32_e32 v70, v170, v70, vcc
	v_cmp_lt_i32_e32 vcc, v71, v72
	v_lshlrev_b32_e32 v67, 2, v67
	v_lshlrev_b32_e32 v68, 2, v68
	v_cndmask_b32_e32 v71, v170, v71, vcc
	v_cmp_lt_i32_e32 vcc, v73, v72
	v_lshlrev_b32_e32 v69, 2, v69
	v_lshlrev_b32_e32 v70, 2, v70
	v_cndmask_b32_e32 v72, v170, v73, vcc
	v_lshlrev_b32_e32 v71, 2, v71
	v_lshlrev_b32_e32 v72, 2, v72
	s_mov_b32 s22, s74
